# P1 GEMM K-loop: 4 of the 6 LDS-DMA issues of each 6-load staging segment moved into the following MFMA block (vmcnt 8->4); saddr-form DMA
# baseline (speedup 1.0000x reference)
.LBB0_299:
	ds_read_b128 v[156:159], v151
	ds_read_b128 v[160:163], v151 offset:1024
	ds_read_b128 v[164:167], v151 offset:2048
	ds_read_b128 v[168:171], v151 offset:3072
	ds_read_b128 v[172:175], v152
	ds_read_b128 v[176:179], v152 offset:1024
	ds_read_b128 v[180:183], v152 offset:2048
	ds_read_b128 v[184:187], v152 offset:3072
	s_add_u32 s24, s22, 0xfffc0080
	s_addc_u32 s25, s23, -1
	s_cmp_eq_u32 s52, 12
	s_cselect_b32 s27, s15, s25
	s_cselect_b32 s26, s48, s24
	s_cselect_b32 s25, s13, s51
	s_cselect_b32 s24, s49, s50
	s_add_i32 m0, s21, 0xc000
	ds_read_b128 v[192:195], v153
	ds_read_b128 v[196:199], v153 offset:1024
	ds_read_b128 v[200:203], v153 offset:2048
	ds_read_b128 v[204:207], v153 offset:3072
	ds_read_b128 v[208:211], v153 offset:4096
	ds_read_b128 v[212:215], v153 offset:5120
	ds_read_b128 v[216:219], v153 offset:6144
	ds_read_b128 v[224:227], v153 offset:7168
	global_load_lds_dwordx4 v138, s[22:23]
	s_add_i32 m0, s21, 0xe000
	s_nop 0
	global_load_lds_dwordx4 v140, s[22:23]
	s_waitcnt vmcnt(8)
	s_waitcnt lgkmcnt(0)
	s_barrier
	s_setprio 1
	s_waitcnt lgkmcnt(0)
	v_mfma_f32_16x16x32_bf16 v[126:129], v[156:159], v[192:195], v[126:129]
	v_mfma_f32_16x16x32_bf16 v[122:125], v[164:167], v[192:195], v[122:125]
	v_mfma_f32_16x16x32_bf16 v[114:117], v[156:159], v[200:203], v[114:117]
	v_mfma_f32_16x16x32_bf16 v[106:109], v[164:167], v[200:203], v[106:109]
	v_mfma_f32_16x16x32_bf16 v[98:101], v[156:159], v[208:211], v[98:101]
	v_mfma_f32_16x16x32_bf16 v[90:93], v[164:167], v[208:211], v[90:93]
	v_mfma_f32_16x16x32_bf16 v[82:85], v[156:159], v[216:219], v[82:85]
	v_mfma_f32_16x16x32_bf16 v[74:77], v[164:167], v[216:219], v[74:77]
	v_mfma_f32_16x16x32_bf16 v[126:129], v[160:163], v[196:199], v[126:129]
	v_mfma_f32_16x16x32_bf16 v[122:125], v[168:171], v[196:199], v[122:125]
	v_mfma_f32_16x16x32_bf16 v[114:117], v[160:163], v[204:207], v[114:117]
	v_mfma_f32_16x16x32_bf16 v[106:109], v[168:171], v[204:207], v[106:109]
	v_mfma_f32_16x16x32_bf16 v[98:101], v[160:163], v[212:215], v[98:101]
	v_mfma_f32_16x16x32_bf16 v[90:93], v[168:171], v[212:215], v[90:93]
	v_mfma_f32_16x16x32_bf16 v[82:85], v[160:163], v[224:227], v[82:85]
	v_mfma_f32_16x16x32_bf16 v[74:77], v[168:171], v[224:227], v[74:77]
	s_setprio 0
	s_setprio 1
	v_mfma_f32_16x16x32_bf16 v[118:121], v[172:175], v[192:195], v[118:121]
	v_mfma_f32_16x16x32_bf16 v[110:113], v[180:183], v[192:195], v[110:113]
	v_mfma_f32_16x16x32_bf16 v[102:105], v[172:175], v[200:203], v[102:105]
	v_mfma_f32_16x16x32_bf16 v[94:97], v[180:183], v[200:203], v[94:97]
	v_mfma_f32_16x16x32_bf16 v[86:89], v[172:175], v[208:211], v[86:89]
	v_mfma_f32_16x16x32_bf16 v[78:81], v[180:183], v[208:211], v[78:81]
	v_mfma_f32_16x16x32_bf16 v[70:73], v[172:175], v[216:219], v[70:73]
	v_mfma_f32_16x16x32_bf16 v[66:69], v[180:183], v[216:219], v[66:69]
	v_mfma_f32_16x16x32_bf16 v[118:121], v[176:179], v[196:199], v[118:121]
	v_mfma_f32_16x16x32_bf16 v[110:113], v[184:187], v[196:199], v[110:113]
	v_mfma_f32_16x16x32_bf16 v[102:105], v[176:179], v[204:207], v[102:105]
	v_mfma_f32_16x16x32_bf16 v[94:97], v[184:187], v[204:207], v[94:97]
	v_mfma_f32_16x16x32_bf16 v[86:89], v[176:179], v[212:215], v[86:89]
	v_mfma_f32_16x16x32_bf16 v[78:81], v[184:187], v[212:215], v[78:81]
	v_mfma_f32_16x16x32_bf16 v[70:73], v[176:179], v[224:227], v[70:73]
	v_mfma_f32_16x16x32_bf16 v[66:69], v[184:187], v[224:227], v[66:69]
	s_setprio 0
	s_barrier
	s_add_i32 s53, s44, s34
	v_lshl_add_u64 v[148:149], s[24:25], 0, v[134:135]
	s_mov_b32 m0, s53
	ds_read_b128 v[192:195], v153 offset:16384
	ds_read_b128 v[196:199], v153 offset:17408
	ds_read_b128 v[200:203], v153 offset:18432
	ds_read_b128 v[204:207], v153 offset:19456
	ds_read_b128 v[208:211], v153 offset:20480
	ds_read_b128 v[212:215], v153 offset:21504
	ds_read_b128 v[216:219], v153 offset:22528
	ds_read_b128 v[224:227], v153 offset:23552
	global_load_lds_dwordx4 v[148:149], off
	s_add_i32 m0, s53, 0x2000
	s_add_u32 s54, s24, 0x40000
	v_lshl_add_u64 v[188:189], s[24:25], 0, v[130:131]
	s_addc_u32 s55, s25, 0
	s_add_i32 s53, s45, s34
	global_load_lds_dwordx4 v[188:189], off
	v_lshl_add_u64 v[220:221], s[26:27], 0, v[132:133]
	v_lshl_add_u64 v[190:191], s[26:27], 0, v[136:137]
	s_waitcnt vmcnt(4)
	s_waitcnt lgkmcnt(0)
	s_barrier
	s_setprio 1
	s_waitcnt lgkmcnt(0)
	v_mfma_f32_16x16x32_bf16 v[62:65], v[156:159], v[192:195], v[62:65]
	v_mfma_f32_16x16x32_bf16 v[58:61], v[164:167], v[192:195], v[58:61]
	v_mfma_f32_16x16x32_bf16 v[50:53], v[156:159], v[200:203], v[50:53]
	v_mfma_f32_16x16x32_bf16 v[42:45], v[164:167], v[200:203], v[42:45]
	s_mov_b32 m0, s53
	s_nop 0
	global_load_lds_dwordx4 v134, s[54:55]
	v_mfma_f32_16x16x32_bf16 v[34:37], v[156:159], v[208:211], v[34:37]
	v_mfma_f32_16x16x32_bf16 v[26:29], v[164:167], v[208:211], v[26:29]
	v_mfma_f32_16x16x32_bf16 v[18:21], v[156:159], v[216:219], v[18:21]
	v_mfma_f32_16x16x32_bf16 v[10:13], v[164:167], v[216:219], v[10:13]
	v_mfma_f32_16x16x32_bf16 v[62:65], v[160:163], v[196:199], v[62:65]
	v_mfma_f32_16x16x32_bf16 v[58:61], v[168:171], v[196:199], v[58:61]
	v_mfma_f32_16x16x32_bf16 v[50:53], v[160:163], v[204:207], v[50:53]
	v_mfma_f32_16x16x32_bf16 v[42:45], v[168:171], v[204:207], v[42:45]
	s_add_i32 m0, s53, 0x2000
	s_nop 0
	global_load_lds_dwordx4 v130, s[54:55]
	v_mfma_f32_16x16x32_bf16 v[34:37], v[160:163], v[212:215], v[34:37]
	v_mfma_f32_16x16x32_bf16 v[26:29], v[168:171], v[212:215], v[26:29]
	v_mfma_f32_16x16x32_bf16 v[18:21], v[160:163], v[224:227], v[18:21]
	v_mfma_f32_16x16x32_bf16 v[10:13], v[168:171], v[224:227], v[10:13]
	s_setprio 0
	s_setprio 1
	v_mfma_f32_16x16x32_bf16 v[54:57], v[172:175], v[192:195], v[54:57]
	v_mfma_f32_16x16x32_bf16 v[46:49], v[180:183], v[192:195], v[46:49]
	v_mfma_f32_16x16x32_bf16 v[38:41], v[172:175], v[200:203], v[38:41]
	v_mfma_f32_16x16x32_bf16 v[30:33], v[180:183], v[200:203], v[30:33]
	s_mov_b32 m0, s21
	s_nop 0
	global_load_lds_dwordx4 v[190:191], off
	v_mfma_f32_16x16x32_bf16 v[22:25], v[172:175], v[208:211], v[22:25]
	v_mfma_f32_16x16x32_bf16 v[14:17], v[180:183], v[208:211], v[14:17]
	v_mfma_f32_16x16x32_bf16 v[6:9], v[172:175], v[216:219], v[6:9]
	v_mfma_f32_16x16x32_bf16 v[2:5], v[180:183], v[216:219], v[2:5]
	v_mfma_f32_16x16x32_bf16 v[54:57], v[176:179], v[196:199], v[54:57]
	v_mfma_f32_16x16x32_bf16 v[46:49], v[184:187], v[196:199], v[46:49]
	v_mfma_f32_16x16x32_bf16 v[38:41], v[176:179], v[204:207], v[38:41]
	v_mfma_f32_16x16x32_bf16 v[30:33], v[184:187], v[204:207], v[30:33]
	s_mov_b32 m0, s37
	s_nop 0
	global_load_lds_dwordx4 v[220:221], off
	v_mfma_f32_16x16x32_bf16 v[22:25], v[176:179], v[212:215], v[22:25]
	v_mfma_f32_16x16x32_bf16 v[14:17], v[184:187], v[212:215], v[14:17]
	v_mfma_f32_16x16x32_bf16 v[6:9], v[176:179], v[224:227], v[6:9]
	v_mfma_f32_16x16x32_bf16 v[2:5], v[184:187], v[224:227], v[2:5]
	s_setprio 0
	s_barrier
	s_add_i32 s53, 0, 0x18000
	v_add_u32_e32 v146, s53, v147
	s_add_i32 s54, 0, 0x1c000
	ds_read_b128 v[156:159], v146
	ds_read_b128 v[160:163], v146 offset:1024
	ds_read_b128 v[164:167], v146 offset:2048
	ds_read_b128 v[168:171], v146 offset:3072
	v_add_u32_e32 v146, s54, v147
	ds_read_b128 v[172:175], v146
	ds_read_b128 v[176:179], v146 offset:1024
	ds_read_b128 v[180:183], v146 offset:2048
	ds_read_b128 v[184:187], v146 offset:3072
	s_add_u32 s26, s26, 0x40000
	s_addc_u32 s27, s27, 0
	s_mov_b32 m0, s38
	ds_read_b128 v[192:195], v153 offset:32768
	ds_read_b128 v[196:199], v153 offset:33792
	ds_read_b128 v[200:203], v153 offset:34816
	ds_read_b128 v[204:207], v153 offset:35840
	ds_read_b128 v[208:211], v153 offset:36864
	ds_read_b128 v[212:215], v153 offset:37888
	ds_read_b128 v[216:219], v153 offset:38912
	ds_read_b128 v[224:227], v153 offset:39936
	global_load_lds_dwordx4 v136, s[26:27]
	v_lshl_add_u64 v[228:229], s[26:27], 0, v[132:133]
	s_mov_b32 m0, s39
	s_nop 0
	global_load_lds_dwordx4 v[228:229], off
	s_waitcnt vmcnt(8)
	s_waitcnt lgkmcnt(0)
	s_barrier
	s_setprio 1
	s_waitcnt lgkmcnt(0)
	v_mfma_f32_16x16x32_bf16 v[126:129], v[156:159], v[192:195], v[126:129]
	v_mfma_f32_16x16x32_bf16 v[122:125], v[164:167], v[192:195], v[122:125]
	v_mfma_f32_16x16x32_bf16 v[114:117], v[156:159], v[200:203], v[114:117]
	v_mfma_f32_16x16x32_bf16 v[106:109], v[164:167], v[200:203], v[106:109]
	v_mfma_f32_16x16x32_bf16 v[98:101], v[156:159], v[208:211], v[98:101]
	v_mfma_f32_16x16x32_bf16 v[90:93], v[164:167], v[208:211], v[90:93]
	v_mfma_f32_16x16x32_bf16 v[82:85], v[156:159], v[216:219], v[82:85]
	v_mfma_f32_16x16x32_bf16 v[74:77], v[164:167], v[216:219], v[74:77]
	v_mfma_f32_16x16x32_bf16 v[126:129], v[160:163], v[196:199], v[126:129]
	v_mfma_f32_16x16x32_bf16 v[122:125], v[168:171], v[196:199], v[122:125]
	v_mfma_f32_16x16x32_bf16 v[114:117], v[160:163], v[204:207], v[114:117]
	v_mfma_f32_16x16x32_bf16 v[106:109], v[168:171], v[204:207], v[106:109]
	v_mfma_f32_16x16x32_bf16 v[98:101], v[160:163], v[212:215], v[98:101]
	v_mfma_f32_16x16x32_bf16 v[90:93], v[168:171], v[212:215], v[90:93]
	v_mfma_f32_16x16x32_bf16 v[82:85], v[160:163], v[224:227], v[82:85]
	v_mfma_f32_16x16x32_bf16 v[74:77], v[168:171], v[224:227], v[74:77]
	s_setprio 0
	s_setprio 1
	v_mfma_f32_16x16x32_bf16 v[118:121], v[172:175], v[192:195], v[118:121]
	v_mfma_f32_16x16x32_bf16 v[110:113], v[180:183], v[192:195], v[110:113]
	v_mfma_f32_16x16x32_bf16 v[102:105], v[172:175], v[200:203], v[102:105]
	v_mfma_f32_16x16x32_bf16 v[94:97], v[180:183], v[200:203], v[94:97]
	v_mfma_f32_16x16x32_bf16 v[86:89], v[172:175], v[208:211], v[86:89]
	v_mfma_f32_16x16x32_bf16 v[78:81], v[180:183], v[208:211], v[78:81]
	v_mfma_f32_16x16x32_bf16 v[70:73], v[172:175], v[216:219], v[70:73]
	v_mfma_f32_16x16x32_bf16 v[66:69], v[180:183], v[216:219], v[66:69]
	v_mfma_f32_16x16x32_bf16 v[118:121], v[176:179], v[196:199], v[118:121]
	v_mfma_f32_16x16x32_bf16 v[110:113], v[184:187], v[196:199], v[110:113]
	v_mfma_f32_16x16x32_bf16 v[102:105], v[176:179], v[204:207], v[102:105]
	v_mfma_f32_16x16x32_bf16 v[94:97], v[184:187], v[204:207], v[94:97]
	v_mfma_f32_16x16x32_bf16 v[86:89], v[176:179], v[212:215], v[86:89]
	v_mfma_f32_16x16x32_bf16 v[78:81], v[184:187], v[212:215], v[78:81]
	v_mfma_f32_16x16x32_bf16 v[70:73], v[176:179], v[224:227], v[70:73]
	v_mfma_f32_16x16x32_bf16 v[66:69], v[184:187], v[224:227], v[66:69]
	s_setprio 0
	s_barrier
	s_add_i32 s26, s53, s34
	v_lshl_add_u64 v[148:149], v[148:149], 0, s[8:9]
	s_mov_b32 m0, s26
	ds_read_b128 v[192:195], v153 offset:49152
	ds_read_b128 v[196:199], v153 offset:50176
	ds_read_b128 v[200:203], v153 offset:51200
	ds_read_b128 v[204:207], v153 offset:52224
	ds_read_b128 v[208:211], v153 offset:53248
	ds_read_b128 v[212:215], v153 offset:54272
	ds_read_b128 v[216:219], v153 offset:55296
	ds_read_b128 v[224:227], v153 offset:56320
	global_load_lds_dwordx4 v[148:149], off
	s_add_i32 m0, s26, 0x2000
	s_add_u32 s24, s24, 0x40080
	v_lshl_add_u64 v[148:149], v[188:189], 0, s[8:9]
	s_addc_u32 s25, s25, 0
	s_add_i32 s26, s54, s34
	global_load_lds_dwordx4 v[148:149], off
	v_lshl_add_u64 v[148:149], v[190:191], 0, s[8:9]
	v_lshl_add_u64 v[228:229], v[220:221], 0, s[8:9]
	s_waitcnt vmcnt(4)
	s_waitcnt lgkmcnt(0)
	s_barrier
	s_setprio 1
	s_waitcnt lgkmcnt(0)
	v_mfma_f32_16x16x32_bf16 v[62:65], v[156:159], v[192:195], v[62:65]
	v_mfma_f32_16x16x32_bf16 v[58:61], v[164:167], v[192:195], v[58:61]
	v_mfma_f32_16x16x32_bf16 v[50:53], v[156:159], v[200:203], v[50:53]
	v_mfma_f32_16x16x32_bf16 v[42:45], v[164:167], v[200:203], v[42:45]
	s_mov_b32 m0, s26
	s_nop 0
	global_load_lds_dwordx4 v134, s[24:25]
	v_mfma_f32_16x16x32_bf16 v[34:37], v[156:159], v[208:211], v[34:37]
	v_mfma_f32_16x16x32_bf16 v[26:29], v[164:167], v[208:211], v[26:29]
	v_mfma_f32_16x16x32_bf16 v[18:21], v[156:159], v[216:219], v[18:21]
	v_mfma_f32_16x16x32_bf16 v[10:13], v[164:167], v[216:219], v[10:13]
	v_mfma_f32_16x16x32_bf16 v[62:65], v[160:163], v[196:199], v[62:65]
	v_mfma_f32_16x16x32_bf16 v[58:61], v[168:171], v[196:199], v[58:61]
	v_mfma_f32_16x16x32_bf16 v[50:53], v[160:163], v[204:207], v[50:53]
	v_mfma_f32_16x16x32_bf16 v[42:45], v[168:171], v[204:207], v[42:45]
	s_add_i32 m0, s26, 0x2000
	s_nop 0
	global_load_lds_dwordx4 v130, s[24:25]
	v_mfma_f32_16x16x32_bf16 v[34:37], v[160:163], v[212:215], v[34:37]
	v_mfma_f32_16x16x32_bf16 v[26:29], v[168:171], v[212:215], v[26:29]
	v_mfma_f32_16x16x32_bf16 v[18:21], v[160:163], v[224:227], v[18:21]
	v_mfma_f32_16x16x32_bf16 v[10:13], v[168:171], v[224:227], v[10:13]
	s_setprio 0
	s_setprio 1
	v_mfma_f32_16x16x32_bf16 v[54:57], v[172:175], v[192:195], v[54:57]
	v_mfma_f32_16x16x32_bf16 v[46:49], v[180:183], v[192:195], v[46:49]
	v_mfma_f32_16x16x32_bf16 v[38:41], v[172:175], v[200:203], v[38:41]
	v_mfma_f32_16x16x32_bf16 v[30:33], v[180:183], v[200:203], v[30:33]
	s_mov_b32 m0, s41
	s_nop 0
	global_load_lds_dwordx4 v[148:149], off
	v_mfma_f32_16x16x32_bf16 v[22:25], v[172:175], v[208:211], v[22:25]
	v_mfma_f32_16x16x32_bf16 v[14:17], v[180:183], v[208:211], v[14:17]
	v_mfma_f32_16x16x32_bf16 v[6:9], v[172:175], v[216:219], v[6:9]
	v_mfma_f32_16x16x32_bf16 v[2:5], v[180:183], v[216:219], v[2:5]
	v_mfma_f32_16x16x32_bf16 v[54:57], v[176:179], v[196:199], v[54:57]
	v_mfma_f32_16x16x32_bf16 v[46:49], v[184:187], v[196:199], v[46:49]
	v_mfma_f32_16x16x32_bf16 v[38:41], v[176:179], v[204:207], v[38:41]
	v_mfma_f32_16x16x32_bf16 v[30:33], v[184:187], v[204:207], v[30:33]
	s_mov_b32 m0, s42
	s_nop 0
	global_load_lds_dwordx4 v[228:229], off
	v_mfma_f32_16x16x32_bf16 v[22:25], v[176:179], v[212:215], v[22:25]
	v_mfma_f32_16x16x32_bf16 v[14:17], v[184:187], v[212:215], v[14:17]
	v_mfma_f32_16x16x32_bf16 v[6:9], v[176:179], v[224:227], v[6:9]
	v_mfma_f32_16x16x32_bf16 v[2:5], v[184:187], v[224:227], v[2:5]
	s_setprio 0
	s_barrier
	s_add_i32 s52, s52, 2
	s_add_u32 s22, s22, 0x100
	s_addc_u32 s23, s23, 0
	s_add_u32 s50, s50, 0x100
	s_addc_u32 s51, s51, 0
	s_cmp_gt_u32 s52, 13
	s_cbranch_scc0 .LBB0_299
	s_and_b64 vcc, exec, s[10:11]
	s_cbranch_vccz .LBB0_302
	s_barrier
